# C1 + router chunk loop: MFMA-block waits no longer drain the next chunk's x prefetch and the U8 stores
# speedup vs baseline: 1.0038x; 1.0038x over previous
.LBB0_1232:
	v_add_u32_e32 v50, s12, v140
	v_ashrrev_i32_e32 v51, 31, v50
	v_lshlrev_b64 v[52:53], 1, v[50:51]
	v_add_u32_e32 v56, 16, v50
	v_lshl_add_u64 v[54:55], v[134:135], 0, v[52:53]
	v_lshl_add_u64 v[52:53], v[136:137], 0, v[52:53]
	v_ashrrev_i32_e32 v57, 31, v56
	global_load_dwordx4 v[74:77], v[54:55], off
	global_load_dwordx4 v[70:73], v[54:55], off offset:32
	v_lshl_add_u64 v[56:57], v[56:57], 1, v[136:137]
	global_load_dwordx4 v[78:81], v[52:53], off
	global_load_dwordx4 v[66:69], v[56:57], off
	v_add_u32_e32 v52, 32, v50
	v_add_u32_e32 v50, 48, v50
	v_ashrrev_i32_e32 v53, 31, v52
	v_ashrrev_i32_e32 v51, 31, v50
	v_add_u32_e32 v111, 0, v122
	v_lshl_add_u64 v[52:53], v[52:53], 1, v[136:137]
	v_lshl_add_u64 v[50:51], v[50:51], 1, v[136:137]
	v_add_u32_e32 v82, 0x1a800, v111
	v_add_u32_e32 v110, 0, v204
	global_load_dwordx4 v[62:65], v[54:55], off offset:64
	s_nop 0
	global_load_dwordx4 v[54:57], v[54:55], off offset:96
	s_nop 0
	global_load_dwordx4 v[58:61], v[52:53], off
	s_nop 0
	global_load_dwordx4 v[50:53], v[50:51], off
	v_add_u32_e32 v83, 0x1a810, v111
	ds_read_b128 v[86:89], v82
	ds_read_b128 v[90:93], v83
	v_add_u32_e32 v82, 0x1c800, v110
	v_add_u32_e32 v94, 0x1c810, v110
	ds_read_b128 v[82:85], v82
	ds_read_b128 v[94:97], v94
	s_waitcnt vmcnt(12)
	v_lshlrev_b32_e32 v102, 16, v26
	v_and_b32_e32 v103, 0xffff0000, v26
	s_waitcnt vmcnt(8)
	v_lshlrev_b32_e32 v114, 16, v38
	v_and_b32_e32 v115, 0xffff0000, v38
	v_lshlrev_b32_e32 v104, 16, v27
	v_and_b32_e32 v105, 0xffff0000, v27
	v_lshlrev_b32_e32 v116, 16, v39
	v_and_b32_e32 v117, 0xffff0000, v39
	v_pk_add_f32 v[154:155], v[102:103], v[114:115]
	v_pk_add_f32 v[152:153], v[104:105], v[116:117]
	s_waitcnt lgkmcnt(3)
	v_pk_mul_f32 v[116:117], v[86:87], v[154:155]
	v_add_u32_e32 v102, 0x1c830, v110
	s_waitcnt lgkmcnt(0)
	v_pk_mul_f32 v[162:163], v[94:95], v[116:117] op_sel:[0,1]
	v_add_u32_e32 v94, 0x1c820, v110
	v_pk_mul_f32 v[160:161], v[96:97], v[116:117] op_sel:[0,1]
	ds_read_b128 v[94:97], v94
	ds_read_b128 v[102:105], v102
	v_pk_mul_f32 v[114:115], v[88:89], v[152:153]
	v_pk_fma_f32 v[82:83], v[82:83], v[116:117], v[162:163] op_sel_hi:[1,0,1]
	v_pk_fma_f32 v[84:85], v[84:85], v[116:117], v[160:161] op_sel_hi:[1,0,1]
	s_waitcnt lgkmcnt(1)
	v_pk_fma_f32 v[82:83], v[94:95], v[114:115], v[82:83] op_sel_hi:[1,0,1]
	v_pk_fma_f32 v[84:85], v[96:97], v[114:115], v[84:85] op_sel_hi:[1,0,1]
	s_waitcnt lgkmcnt(0)
	v_pk_fma_f32 v[82:83], v[102:103], v[114:115], v[82:83] op_sel:[0,1,0]
	v_pk_fma_f32 v[84:85], v[104:105], v[114:115], v[84:85] op_sel:[0,1,0]
	v_pk_add_f32 v[82:83], v[98:99], v[82:83]
	v_pk_add_f32 v[84:85], v[100:101], v[84:85]
	v_add_u32_e32 v94, 0x1c840, v110
	v_add_u32_e32 v98, 0x1c850, v110
	ds_read_b128 v[94:97], v94
	ds_read_b128 v[98:101], v98
	v_lshlrev_b32_e32 v108, 16, v28
	v_and_b32_e32 v109, 0xffff0000, v28
	v_lshlrev_b32_e32 v156, 16, v40
	v_and_b32_e32 v157, 0xffff0000, v40
	v_lshlrev_b32_e32 v112, 16, v29
	v_and_b32_e32 v113, 0xffff0000, v29
	v_lshlrev_b32_e32 v158, 16, v41
	v_and_b32_e32 v159, 0xffff0000, v41
	v_pk_add_f32 v[156:157], v[108:109], v[156:157]
	v_pk_add_f32 v[158:159], v[112:113], v[158:159]
	v_pk_mul_f32 v[112:113], v[90:91], v[156:157]
	v_add_u32_e32 v102, 0x1c870, v110
	s_waitcnt lgkmcnt(0)
	v_pk_mul_f32 v[162:163], v[98:99], v[112:113] op_sel:[0,1]
	v_add_u32_e32 v98, 0x1c860, v110
	v_pk_mul_f32 v[160:161], v[100:101], v[112:113] op_sel:[0,1]
	ds_read_b128 v[98:101], v98
	ds_read_b128 v[102:105], v102
	v_pk_mul_f32 v[108:109], v[92:93], v[158:159]
	v_pk_fma_f32 v[94:95], v[94:95], v[112:113], v[162:163] op_sel_hi:[1,0,1]
	v_pk_fma_f32 v[96:97], v[96:97], v[112:113], v[160:161] op_sel_hi:[1,0,1]
	s_waitcnt lgkmcnt(1)
	v_pk_fma_f32 v[94:95], v[98:99], v[108:109], v[94:95] op_sel_hi:[1,0,1]
	v_pk_fma_f32 v[96:97], v[100:101], v[108:109], v[96:97] op_sel_hi:[1,0,1]
	s_waitcnt lgkmcnt(0)
	v_pk_fma_f32 v[94:95], v[102:103], v[108:109], v[94:95] op_sel:[0,1,0]
	v_pk_fma_f32 v[96:97], v[104:105], v[108:109], v[96:97] op_sel:[0,1,0]
	v_pk_add_f32 v[94:95], v[82:83], v[94:95]
	v_pk_add_f32 v[96:97], v[84:85], v[96:97]
	v_lshl_add_u64 v[106:107], s[26:27], 0, v[146:147]
	v_cvt_pk_bf16_f32 v82, v116, v117
	v_cvt_pk_bf16_f32 v83, v114, v115
	v_cvt_pk_bf16_f32 v84, v112, v113
	v_cvt_pk_bf16_f32 v85, v108, v109
	v_add_co_u32_e32 v172, vcc, s79, v106
	v_lshlrev_b32_e32 v98, 16, v83
	v_and_b32_e32 v99, 0xffff0000, v83
	v_lshlrev_b32_e32 v100, 16, v82
	v_and_b32_e32 v101, 0xffff0000, v82
	v_xor_b32_e32 v99, 0x80000000, v99
	v_xor_b32_e32 v98, 0x80000000, v98
	v_lshlrev_b32_e32 v104, 16, v85
	v_and_b32_e32 v105, 0xffff0000, v85
	v_pk_fma_f32 v[88:89], v[88:89], v[152:153], v[98:99]
	v_xor_b32_e32 v99, 0x80000000, v101
	v_xor_b32_e32 v98, 0x80000000, v100
	v_lshlrev_b32_e32 v102, 16, v84
	v_and_b32_e32 v103, 0xffff0000, v84
	v_pk_fma_f32 v[86:87], v[86:87], v[154:155], v[98:99]
	v_xor_b32_e32 v99, 0x80000000, v105
	v_xor_b32_e32 v98, 0x80000000, v104
	v_pk_fma_f32 v[92:93], v[92:93], v[158:159], v[98:99]
	v_xor_b32_e32 v99, 0x80000000, v103
	v_xor_b32_e32 v98, 0x80000000, v102
	v_pk_fma_f32 v[90:91], v[90:91], v[156:157], v[98:99]
	v_cvt_pk_bf16_f32 v86, v86, v87
	v_cvt_pk_bf16_f32 v87, v88, v89
	v_pk_mul_f32 v[100:101], v[148:149], v[112:113]
	v_cvt_pk_bf16_f32 v88, v90, v91
	v_cvt_pk_bf16_f32 v89, v92, v93
	v_pk_mul_f32 v[92:93], v[148:149], v[116:117]
	v_pk_mul_f32 v[90:91], v[150:151], v[114:115]
	v_rndne_f32_e32 v93, v93
	v_rndne_f32_e32 v92, v92
	v_med3_f32 v93, v93, s75, v201
	v_rndne_f32_e32 v90, v90
	v_rndne_f32_e32 v91, v91
	v_med3_f32 v92, v92, s75, v201
	v_cvt_i32_f32_e32 v93, v93
	v_med3_f32 v90, v90, s75, v201
	v_med3_f32 v91, v91, s75, v201
	v_cvt_i32_f32_e32 v92, v92
	v_cvt_i32_f32_sdwa v90, v90 dst_sel:WORD_1 dst_unused:UNUSED_PAD src0_sel:DWORD
	v_cvt_i32_f32_e32 v91, v91
	v_lshlrev_b32_e32 v93, 8, v93
	v_pk_mul_f32 v[98:99], v[150:151], v[108:109]
	v_and_b32_e32 v93, 0xff00, v93
	v_and_b32_e32 v90, 0xff0000, v90
	v_perm_b32 v91, v91, v92, s78
	v_rndne_f32_e32 v92, v101
	v_or3_b32 v90, v91, v93, v90
	v_rndne_f32_e32 v91, v100
	v_med3_f32 v92, v92, s75, v201
	v_rndne_f32_e32 v93, v98
	v_rndne_f32_e32 v98, v99
	v_med3_f32 v91, v91, s75, v201
	v_cvt_i32_f32_e32 v92, v92
	v_med3_f32 v93, v93, s75, v201
	v_med3_f32 v98, v98, s75, v201
	v_cvt_i32_f32_e32 v91, v91
	v_cvt_i32_f32_sdwa v93, v93 dst_sel:WORD_1 dst_unused:UNUSED_PAD src0_sel:DWORD
	v_cvt_i32_f32_e32 v98, v98
	v_lshlrev_b32_e32 v92, 8, v92
	v_and_b32_e32 v92, 0xff00, v92
	v_and_b32_e32 v93, 0xff0000, v93
	v_perm_b32 v91, v98, v91, s78
	v_or3_b32 v91, v91, v92, v93
	v_addc_co_u32_e32 v173, vcc, 0, v107, vcc
	global_store_dwordx2 v[172:173], v[90:91], off
	v_add_u32_e32 v90, 0x1a820, v111
	v_add_u32_e32 v91, 0x1a830, v111
	ds_read_b128 v[98:101], v90
	ds_read_b128 v[102:105], v91
	v_add_u32_e32 v90, 0x1c880, v110
	v_add_u32_e32 v106, 0x1c890, v110
	ds_read_b128 v[90:93], v90
	ds_read_b128 v[106:109], v106
	v_lshlrev_b32_e32 v112, 16, v22
	v_and_b32_e32 v113, 0xffff0000, v22
	v_lshlrev_b32_e32 v162, 16, v46
	v_and_b32_e32 v163, 0xffff0000, v46
	v_pk_add_f32 v[162:163], v[112:113], v[162:163]
	v_lshlrev_b32_e32 v114, 16, v23
	s_waitcnt lgkmcnt(3)
	v_pk_mul_f32 v[174:175], v[98:99], v[162:163]
	v_and_b32_e32 v115, 0xffff0000, v23
	s_waitcnt lgkmcnt(0)
	v_pk_mul_f32 v[178:179], v[106:107], v[174:175] op_sel:[0,1]
	v_add_u32_e32 v106, 0x1c8a0, v110
	v_lshlrev_b32_e32 v164, 16, v47
	v_and_b32_e32 v165, 0xffff0000, v47
	v_pk_mul_f32 v[176:177], v[108:109], v[174:175] op_sel:[0,1]
	ds_read_b128 v[106:109], v106
	v_add_u32_e32 v112, 0x1c8b0, v110
	v_pk_add_f32 v[164:165], v[114:115], v[164:165]
	ds_read_b128 v[112:115], v112
	v_pk_mul_f32 v[170:171], v[100:101], v[164:165]
	v_pk_fma_f32 v[90:91], v[90:91], v[174:175], v[178:179] op_sel_hi:[1,0,1]
	v_pk_fma_f32 v[92:93], v[92:93], v[174:175], v[176:177] op_sel_hi:[1,0,1]
	s_waitcnt lgkmcnt(1)
	v_pk_fma_f32 v[90:91], v[106:107], v[170:171], v[90:91] op_sel_hi:[1,0,1]
	v_pk_fma_f32 v[92:93], v[108:109], v[170:171], v[92:93] op_sel_hi:[1,0,1]
	s_waitcnt lgkmcnt(0)
	v_pk_fma_f32 v[90:91], v[112:113], v[170:171], v[90:91] op_sel:[0,1,0]
	v_pk_fma_f32 v[92:93], v[114:115], v[170:171], v[92:93] op_sel:[0,1,0]
	v_pk_add_f32 v[90:91], v[94:95], v[90:91]
	v_pk_add_f32 v[92:93], v[96:97], v[92:93]
	v_add_u32_e32 v94, 0x1c8c0, v110
	v_add_u32_e32 v106, 0x1c8d0, v110
	ds_read_b128 v[94:97], v94
	ds_read_b128 v[106:109], v106
	v_lshlrev_b32_e32 v116, 16, v24
	v_and_b32_e32 v117, 0xffff0000, v24
	v_lshlrev_b32_e32 v166, 16, v48
	v_and_b32_e32 v167, 0xffff0000, v48
	v_lshlrev_b32_e32 v160, 16, v25
	v_and_b32_e32 v161, 0xffff0000, v25
	v_lshlrev_b32_e32 v168, 16, v49
	v_and_b32_e32 v169, 0xffff0000, v49
	v_pk_add_f32 v[166:167], v[116:117], v[166:167]
	v_pk_add_f32 v[160:161], v[160:161], v[168:169]
	v_pk_mul_f32 v[168:169], v[102:103], v[166:167]
	v_add_u32_e32 v112, 0x1c8f0, v110
	s_waitcnt lgkmcnt(0)
	v_pk_mul_f32 v[178:179], v[106:107], v[168:169] op_sel:[0,1]
	v_add_u32_e32 v106, 0x1c8e0, v110
	v_pk_mul_f32 v[176:177], v[108:109], v[168:169] op_sel:[0,1]
	ds_read_b128 v[106:109], v106
	ds_read_b128 v[112:115], v112
	v_pk_mul_f32 v[116:117], v[104:105], v[160:161]
	v_pk_fma_f32 v[94:95], v[94:95], v[168:169], v[178:179] op_sel_hi:[1,0,1]
	v_pk_fma_f32 v[96:97], v[96:97], v[168:169], v[176:177] op_sel_hi:[1,0,1]
	s_waitcnt lgkmcnt(1)
	v_pk_fma_f32 v[94:95], v[106:107], v[116:117], v[94:95] op_sel_hi:[1,0,1]
	v_pk_fma_f32 v[96:97], v[108:109], v[116:117], v[96:97] op_sel_hi:[1,0,1]
	s_waitcnt lgkmcnt(0)
	v_pk_fma_f32 v[94:95], v[112:113], v[116:117], v[94:95] op_sel:[0,1,0]
	v_pk_fma_f32 v[96:97], v[114:115], v[116:117], v[96:97] op_sel:[0,1,0]
	v_pk_add_f32 v[106:107], v[90:91], v[94:95]
	v_pk_add_f32 v[108:109], v[92:93], v[96:97]
	v_lshlrev_b32_e32 v178, 16, v42
	v_cvt_pk_bf16_f32 v90, v174, v175
	v_cvt_pk_bf16_f32 v91, v170, v171
	v_cvt_pk_bf16_f32 v92, v168, v169
	v_cvt_pk_bf16_f32 v93, v116, v117
	v_and_b32_e32 v179, 0xffff0000, v42
	v_lshlrev_b32_e32 v94, 16, v91
	v_and_b32_e32 v95, 0xffff0000, v91
	v_lshlrev_b32_e32 v112, 16, v90
	v_and_b32_e32 v113, 0xffff0000, v90
	v_lshlrev_b32_e32 v114, 16, v92
	v_and_b32_e32 v115, 0xffff0000, v92
	v_xor_b32_e32 v95, 0x80000000, v95
	v_xor_b32_e32 v94, 0x80000000, v94
	v_lshlrev_b32_e32 v145, 16, v93
	v_and_b32_e32 v176, 0xffff0000, v93
	v_pk_fma_f32 v[96:97], v[100:101], v[164:165], v[94:95]
	v_xor_b32_e32 v95, 0x80000000, v113
	v_xor_b32_e32 v94, 0x80000000, v112
	v_xor_b32_e32 v101, 0x80000000, v115
	v_xor_b32_e32 v100, 0x80000000, v114
	v_pk_fma_f32 v[94:95], v[98:99], v[162:163], v[94:95]
	v_xor_b32_e32 v99, 0x80000000, v176
	v_xor_b32_e32 v98, 0x80000000, v145
	v_pk_fma_f32 v[100:101], v[102:103], v[166:167], v[100:101]
	v_pk_fma_f32 v[98:99], v[104:105], v[160:161], v[98:99]
	v_cvt_pk_bf16_f32 v94, v94, v95
	v_cvt_pk_bf16_f32 v95, v96, v97
	v_cvt_pk_bf16_f32 v96, v100, v101
	v_pk_mul_f32 v[100:101], v[148:149], v[174:175]
	v_cvt_pk_bf16_f32 v97, v98, v99
	v_pk_mul_f32 v[98:99], v[150:151], v[170:171]
	v_rndne_f32_e32 v101, v101
	v_rndne_f32_e32 v100, v100
	v_med3_f32 v101, v101, s75, v201
	v_rndne_f32_e32 v98, v98
	v_rndne_f32_e32 v99, v99
	v_med3_f32 v100, v100, s75, v201
	v_cvt_i32_f32_e32 v101, v101
	v_med3_f32 v98, v98, s75, v201
	v_med3_f32 v99, v99, s75, v201
	v_cvt_i32_f32_e32 v100, v100
	v_cvt_i32_f32_sdwa v98, v98 dst_sel:WORD_1 dst_unused:UNUSED_PAD src0_sel:DWORD
	v_cvt_i32_f32_e32 v99, v99
	v_pk_mul_f32 v[104:105], v[148:149], v[168:169]
	v_lshlrev_b32_e32 v101, 8, v101
	v_pk_mul_f32 v[102:103], v[150:151], v[116:117]
	v_and_b32_e32 v101, 0xff00, v101
	v_and_b32_e32 v98, 0xff0000, v98
	v_perm_b32 v99, v99, v100, s78
	v_rndne_f32_e32 v100, v105
	v_or3_b32 v98, v99, v101, v98
	v_rndne_f32_e32 v99, v104
	v_med3_f32 v100, v100, s75, v201
	v_rndne_f32_e32 v101, v102
	v_rndne_f32_e32 v102, v103
	v_med3_f32 v99, v99, s75, v201
	v_cvt_i32_f32_e32 v100, v100
	v_med3_f32 v101, v101, s75, v201
	v_med3_f32 v102, v102, s75, v201
	v_cvt_i32_f32_e32 v99, v99
	v_cvt_i32_f32_sdwa v101, v101 dst_sel:WORD_1 dst_unused:UNUSED_PAD src0_sel:DWORD
	v_cvt_i32_f32_e32 v102, v102
	v_lshlrev_b32_e32 v100, 8, v100
	v_and_b32_e32 v100, 0xff00, v100
	v_and_b32_e32 v101, 0xff0000, v101
	v_perm_b32 v99, v102, v99, s78
	v_or3_b32 v99, v99, v100, v101
	global_store_dwordx2 v[172:173], v[98:99], off offset:8
	v_add_u32_e32 v98, 0x1a840, v111
	v_add_u32_e32 v102, 0x1a850, v111
	ds_read_b128 v[98:101], v98
	ds_read_b128 v[112:115], v102
	v_add_u32_e32 v102, 0x1c900, v110
	v_add_u32_e32 v145, 0x1c910, v110
	ds_read_b128 v[102:105], v102
	ds_read_b128 v[174:177], v145
	v_lshlrev_b32_e32 v116, 16, v18
	v_and_b32_e32 v117, 0xffff0000, v18
	v_lshlrev_b32_e32 v168, 16, v19
	v_and_b32_e32 v169, 0xffff0000, v19
	v_lshlrev_b32_e32 v170, 16, v43
	v_and_b32_e32 v171, 0xffff0000, v43
	v_pk_add_f32 v[170:171], v[168:169], v[170:171]
	v_pk_add_f32 v[168:169], v[116:117], v[178:179]
	v_add_u32_e32 v145, 0x1c920, v110
	s_waitcnt lgkmcnt(3)
	v_pk_mul_f32 v[210:211], v[98:99], v[168:169]
	v_pk_mul_f32 v[116:117], v[100:101], v[170:171]
	s_waitcnt lgkmcnt(0)
	v_pk_mul_f32 v[212:213], v[176:177], v[210:211] op_sel:[0,1]
	v_pk_mul_f32 v[214:215], v[174:175], v[210:211] op_sel:[0,1]
	ds_read_b128 v[174:177], v145
	v_add_u32_e32 v145, 0x1c930, v110
	ds_read_b128 v[178:181], v145
	v_pk_fma_f32 v[102:103], v[102:103], v[210:211], v[214:215] op_sel_hi:[1,0,1]
	v_pk_fma_f32 v[104:105], v[104:105], v[210:211], v[212:213] op_sel_hi:[1,0,1]
	s_waitcnt lgkmcnt(1)
	v_pk_fma_f32 v[102:103], v[174:175], v[116:117], v[102:103] op_sel_hi:[1,0,1]
	v_pk_fma_f32 v[104:105], v[176:177], v[116:117], v[104:105] op_sel_hi:[1,0,1]
	s_waitcnt lgkmcnt(0)
	v_pk_fma_f32 v[102:103], v[178:179], v[116:117], v[102:103] op_sel:[0,1,0]
	v_pk_fma_f32 v[104:105], v[180:181], v[116:117], v[104:105] op_sel:[0,1,0]
	v_pk_add_f32 v[102:103], v[106:107], v[102:103]
	v_pk_add_f32 v[104:105], v[108:109], v[104:105]
	v_add_u32_e32 v106, 0x1c940, v110
	v_add_u32_e32 v145, 0x1c950, v110
	ds_read_b128 v[106:109], v106
	ds_read_b128 v[178:181], v145
	v_lshlrev_b32_e32 v182, 16, v20
	v_and_b32_e32 v183, 0xffff0000, v20
	v_lshlrev_b32_e32 v206, 16, v44
	v_and_b32_e32 v207, 0xffff0000, v44
	v_lshlrev_b32_e32 v184, 16, v21
	v_and_b32_e32 v185, 0xffff0000, v21
	v_lshlrev_b32_e32 v208, 16, v45
	v_and_b32_e32 v209, 0xffff0000, v45
	v_pk_add_f32 v[176:177], v[182:183], v[206:207]
	v_pk_add_f32 v[174:175], v[184:185], v[208:209]
	v_pk_mul_f32 v[208:209], v[112:113], v[176:177]
	v_add_u32_e32 v145, 0x1c960, v110
	s_waitcnt lgkmcnt(0)
	v_pk_mul_f32 v[212:213], v[180:181], v[208:209] op_sel:[0,1]
	v_pk_mul_f32 v[214:215], v[178:179], v[208:209] op_sel:[0,1]
	ds_read_b128 v[178:181], v145
	v_add_u32_e32 v145, 0x1c970, v110
	ds_read_b128 v[182:185], v145
	v_pk_mul_f32 v[206:207], v[114:115], v[174:175]
	v_pk_fma_f32 v[106:107], v[106:107], v[208:209], v[214:215] op_sel_hi:[1,0,1]
	v_pk_fma_f32 v[108:109], v[108:109], v[208:209], v[212:213] op_sel_hi:[1,0,1]
	s_waitcnt lgkmcnt(1)
	v_pk_fma_f32 v[106:107], v[178:179], v[206:207], v[106:107] op_sel_hi:[1,0,1]
	v_pk_fma_f32 v[108:109], v[180:181], v[206:207], v[108:109] op_sel_hi:[1,0,1]
	s_waitcnt lgkmcnt(0)
	v_pk_fma_f32 v[106:107], v[182:183], v[206:207], v[106:107] op_sel:[0,1,0]
	v_pk_fma_f32 v[108:109], v[184:185], v[206:207], v[108:109] op_sel:[0,1,0]
	v_pk_add_f32 v[182:183], v[102:103], v[106:107]
	v_pk_add_f32 v[184:185], v[104:105], v[108:109]
	v_lshlrev_b32_e32 v214, 16, v34
	v_cvt_pk_bf16_f32 v102, v210, v211
	v_cvt_pk_bf16_f32 v103, v116, v117
	v_cvt_pk_bf16_f32 v104, v208, v209
	v_cvt_pk_bf16_f32 v105, v206, v207
	v_and_b32_e32 v215, 0xffff0000, v34
	v_lshlrev_b32_e32 v106, 16, v103
	v_and_b32_e32 v107, 0xffff0000, v103
	v_lshlrev_b32_e32 v108, 16, v102
	v_and_b32_e32 v109, 0xffff0000, v102
	v_xor_b32_e32 v107, 0x80000000, v107
	v_xor_b32_e32 v106, 0x80000000, v106
	v_lshlrev_b32_e32 v179, 16, v105
	v_and_b32_e32 v180, 0xffff0000, v105
	v_pk_fma_f32 v[100:101], v[100:101], v[170:171], v[106:107]
	v_xor_b32_e32 v107, 0x80000000, v109
	v_xor_b32_e32 v106, 0x80000000, v108
	v_lshlrev_b32_e32 v145, 16, v104
	v_and_b32_e32 v178, 0xffff0000, v104
	v_pk_fma_f32 v[98:99], v[98:99], v[168:169], v[106:107]
	v_xor_b32_e32 v107, 0x80000000, v180
	v_xor_b32_e32 v106, 0x80000000, v179
	v_pk_fma_f32 v[114:115], v[114:115], v[174:175], v[106:107]
	v_xor_b32_e32 v107, 0x80000000, v178
	v_xor_b32_e32 v106, 0x80000000, v145
	v_pk_fma_f32 v[108:109], v[112:113], v[176:177], v[106:107]
	v_cvt_pk_bf16_f32 v106, v98, v99
	v_cvt_pk_bf16_f32 v107, v100, v101
	v_pk_mul_f32 v[100:101], v[148:149], v[210:211]
	v_pk_mul_f32 v[98:99], v[150:151], v[116:117]
	v_rndne_f32_e32 v101, v101
	v_rndne_f32_e32 v100, v100
	v_med3_f32 v101, v101, s75, v201
	v_rndne_f32_e32 v98, v98
	v_rndne_f32_e32 v99, v99
	v_med3_f32 v100, v100, s75, v201
	v_cvt_i32_f32_e32 v101, v101
	v_med3_f32 v98, v98, s75, v201
	v_med3_f32 v99, v99, s75, v201
	v_cvt_i32_f32_e32 v100, v100
	v_cvt_i32_f32_sdwa v98, v98 dst_sel:WORD_1 dst_unused:UNUSED_PAD src0_sel:DWORD
	v_cvt_i32_f32_e32 v99, v99
	v_cvt_pk_bf16_f32 v108, v108, v109
	v_cvt_pk_bf16_f32 v109, v114, v115
	v_pk_mul_f32 v[114:115], v[148:149], v[208:209]
	v_lshlrev_b32_e32 v101, 8, v101
	v_pk_mul_f32 v[112:113], v[150:151], v[206:207]
	v_and_b32_e32 v101, 0xff00, v101
	v_and_b32_e32 v98, 0xff0000, v98
	v_perm_b32 v99, v99, v100, s78
	v_rndne_f32_e32 v100, v115
	v_or3_b32 v98, v99, v101, v98
	v_rndne_f32_e32 v99, v114
	v_med3_f32 v100, v100, s75, v201
	v_rndne_f32_e32 v101, v112
	v_rndne_f32_e32 v112, v113
	v_med3_f32 v99, v99, s75, v201
	v_cvt_i32_f32_e32 v100, v100
	v_med3_f32 v101, v101, s75, v201
	v_med3_f32 v112, v112, s75, v201
	v_cvt_i32_f32_e32 v99, v99
	v_cvt_i32_f32_sdwa v101, v101 dst_sel:WORD_1 dst_unused:UNUSED_PAD src0_sel:DWORD
	v_cvt_i32_f32_e32 v112, v112
	v_lshlrev_b32_e32 v100, 8, v100
	v_and_b32_e32 v100, 0xff00, v100
	v_and_b32_e32 v101, 0xff0000, v101
	v_perm_b32 v99, v112, v99, s78
	v_or3_b32 v99, v99, v100, v101
	global_store_dwordx2 v[172:173], v[98:99], off offset:16
	v_add_u32_e32 v98, 0x1a860, v111
	v_add_u32_e32 v99, 0x1a870, v111
	ds_read_b128 v[114:117], v98
	ds_read_b128 v[206:209], v99
	v_add_u32_e32 v98, 0x1c980, v110
	v_add_u32_e32 v111, 0x1c990, v110
	ds_read_b128 v[98:101], v98
	ds_read_b128 v[210:213], v111
	v_lshlrev_b32_e32 v112, 16, v30
	v_and_b32_e32 v113, 0xffff0000, v30
	v_lshlrev_b32_e32 v178, 16, v31
	v_and_b32_e32 v179, 0xffff0000, v31
	v_lshlrev_b32_e32 v180, 16, v35
	v_and_b32_e32 v181, 0xffff0000, v35
	v_pk_add_f32 v[180:181], v[178:179], v[180:181]
	v_pk_add_f32 v[178:179], v[112:113], v[214:215]
	v_add_u32_e32 v111, 0x1c9a0, v110
	s_waitcnt lgkmcnt(3)
	v_pk_mul_f32 v[228:229], v[114:115], v[178:179]
	v_pk_mul_f32 v[226:227], v[116:117], v[180:181]
	s_waitcnt lgkmcnt(0)
	v_pk_mul_f32 v[112:113], v[212:213], v[228:229] op_sel:[0,1]
	v_pk_mul_f32 v[230:231], v[210:211], v[228:229] op_sel:[0,1]
	ds_read_b128 v[210:213], v111
	v_add_u32_e32 v111, 0x1c9b0, v110
	ds_read_b128 v[214:217], v111
	v_pk_fma_f32 v[98:99], v[98:99], v[228:229], v[230:231] op_sel_hi:[1,0,1]
	v_pk_fma_f32 v[100:101], v[100:101], v[228:229], v[112:113] op_sel_hi:[1,0,1]
	s_waitcnt lgkmcnt(1)
	v_pk_fma_f32 v[98:99], v[210:211], v[226:227], v[98:99] op_sel_hi:[1,0,1]
	v_pk_fma_f32 v[100:101], v[212:213], v[226:227], v[100:101] op_sel_hi:[1,0,1]
	s_waitcnt lgkmcnt(0)
	v_pk_fma_f32 v[98:99], v[214:215], v[226:227], v[98:99] op_sel:[0,1,0]
	v_pk_fma_f32 v[100:101], v[216:217], v[226:227], v[100:101] op_sel:[0,1,0]
	v_pk_add_f32 v[98:99], v[182:183], v[98:99]
	v_pk_add_f32 v[100:101], v[184:185], v[100:101]
	v_add_u32_e32 v111, 0x1c9c0, v110
	v_add_u32_e32 v112, 0x1c9d0, v110
	ds_read_b128 v[210:213], v111
	ds_read_b128 v[214:217], v112
	v_lshlrev_b32_e32 v218, 16, v32
	v_and_b32_e32 v219, 0xffff0000, v32
	v_lshlrev_b32_e32 v222, 16, v36
	v_and_b32_e32 v223, 0xffff0000, v36
	v_lshlrev_b32_e32 v220, 16, v33
	v_and_b32_e32 v221, 0xffff0000, v33
	v_lshlrev_b32_e32 v224, 16, v37
	v_and_b32_e32 v225, 0xffff0000, v37
	v_pk_add_f32 v[184:185], v[218:219], v[222:223]
	v_pk_add_f32 v[182:183], v[220:221], v[224:225]
	v_pk_mul_f32 v[220:221], v[206:207], v[184:185]
	v_add_u32_e32 v111, 0x1c9e0, v110
	s_waitcnt lgkmcnt(0)
	v_pk_mul_f32 v[222:223], v[216:217], v[220:221] op_sel:[0,1]
	v_pk_mul_f32 v[224:225], v[214:215], v[220:221] op_sel:[0,1]
	ds_read_b128 v[214:217], v111
	v_add_u32_e32 v110, 0x1c9f0, v110
	ds_read_b128 v[110:113], v110
	v_pk_mul_f32 v[218:219], v[208:209], v[182:183]
	v_pk_fma_f32 v[210:211], v[210:211], v[220:221], v[224:225] op_sel_hi:[1,0,1]
	v_pk_fma_f32 v[212:213], v[212:213], v[220:221], v[222:223] op_sel_hi:[1,0,1]
	s_waitcnt lgkmcnt(1)
	v_pk_fma_f32 v[210:211], v[214:215], v[218:219], v[210:211] op_sel_hi:[1,0,1]
	v_pk_fma_f32 v[212:213], v[216:217], v[218:219], v[212:213] op_sel_hi:[1,0,1]
	s_waitcnt lgkmcnt(0)
	v_pk_fma_f32 v[110:111], v[110:111], v[218:219], v[210:211] op_sel:[0,1,0]
	v_pk_fma_f32 v[112:113], v[112:113], v[218:219], v[212:213] op_sel:[0,1,0]
	v_pk_add_f32 v[98:99], v[98:99], v[110:111]
	v_pk_add_f32 v[100:101], v[100:101], v[112:113]
	s_cmpk_eq_i32 s12, 0x600
	v_cvt_pk_bf16_f32 v110, v228, v229
	v_cvt_pk_bf16_f32 v111, v226, v227
	v_cvt_pk_bf16_f32 v112, v220, v221
	v_cvt_pk_bf16_f32 v113, v218, v219
	s_nop 0
	v_lshlrev_b32_e32 v210, 16, v111
	v_and_b32_e32 v211, 0xffff0000, v111
	v_lshlrev_b32_e32 v145, 16, v110
	v_and_b32_e32 v205, 0xffff0000, v110
	v_xor_b32_e32 v211, 0x80000000, v211
	v_xor_b32_e32 v210, 0x80000000, v210
	v_lshlrev_b32_e32 v214, 16, v113
	v_and_b32_e32 v215, 0xffff0000, v113
	v_pk_fma_f32 v[116:117], v[116:117], v[180:181], v[210:211]
	v_xor_b32_e32 v211, 0x80000000, v205
	v_xor_b32_e32 v210, 0x80000000, v145
	v_lshlrev_b32_e32 v212, 16, v112
	v_and_b32_e32 v213, 0xffff0000, v112
	v_pk_fma_f32 v[114:115], v[114:115], v[178:179], v[210:211]
	v_xor_b32_e32 v211, 0x80000000, v215
	v_xor_b32_e32 v210, 0x80000000, v214
	v_pk_fma_f32 v[208:209], v[208:209], v[182:183], v[210:211]
	v_xor_b32_e32 v211, 0x80000000, v213
	v_xor_b32_e32 v210, 0x80000000, v212
	v_pk_fma_f32 v[206:207], v[206:207], v[184:185], v[210:211]
	v_cvt_pk_bf16_f32 v114, v114, v115
	v_cvt_pk_bf16_f32 v115, v116, v117
	v_pk_mul_f32 v[212:213], v[148:149], v[220:221]
	v_cvt_pk_bf16_f32 v116, v206, v207
	v_cvt_pk_bf16_f32 v117, v208, v209
	v_pk_mul_f32 v[208:209], v[148:149], v[228:229]
	v_pk_mul_f32 v[206:207], v[150:151], v[226:227]
	v_rndne_f32_e32 v205, v209
	v_rndne_f32_e32 v145, v208
	v_med3_f32 v205, v205, s75, v201
	v_rndne_f32_e32 v206, v206
	v_rndne_f32_e32 v207, v207
	v_med3_f32 v145, v145, s75, v201
	v_cvt_i32_f32_e32 v205, v205
	v_med3_f32 v206, v206, s75, v201
	v_med3_f32 v207, v207, s75, v201
	v_cvt_i32_f32_e32 v145, v145
	v_cvt_i32_f32_sdwa v206, v206 dst_sel:WORD_1 dst_unused:UNUSED_PAD src0_sel:DWORD
	v_cvt_i32_f32_e32 v207, v207
	v_lshlrev_b32_e32 v205, 8, v205
	v_and_b32_e32 v205, 0xff00, v205
	v_and_b32_e32 v206, 0xff0000, v206
	v_perm_b32 v145, v207, v145, s78
	v_pk_mul_f32 v[210:211], v[150:151], v[218:219]
	v_or3_b32 v206, v145, v205, v206
	v_rndne_f32_e32 v205, v213
	v_rndne_f32_e32 v145, v212
	v_med3_f32 v205, v205, s75, v201
	v_rndne_f32_e32 v207, v210
	v_rndne_f32_e32 v208, v211
	v_med3_f32 v145, v145, s75, v201
	v_cvt_i32_f32_e32 v205, v205
	v_med3_f32 v207, v207, s75, v201
	v_med3_f32 v208, v208, s75, v201
	v_cvt_i32_f32_e32 v145, v145
	v_cvt_i32_f32_sdwa v207, v207 dst_sel:WORD_1 dst_unused:UNUSED_PAD src0_sel:DWORD
	v_cvt_i32_f32_e32 v208, v208
	v_lshlrev_b32_e32 v205, 8, v205
	v_and_b32_e32 v205, 0xff00, v205
	v_and_b32_e32 v207, 0xff0000, v207
	v_perm_b32 v145, v208, v145, s78
	v_or3_b32 v207, v145, v205, v207
	global_store_dwordx2 v[172:173], v[206:207], off offset:24
	s_cbranch_scc1 .LBB0_1231
	v_lshl_add_u64 v[26:27], s[26:27], 0, v[142:143]
	v_add_co_u32_e32 v28, vcc, 0x30000000, v26
	v_lshl_add_u64 v[30:31], v[26:27], 0, s[60:61]
	s_nop 0
	v_addc_co_u32_e32 v29, vcc, 0, v27, vcc
	v_add_co_u32_e32 v32, vcc, 0x38000000, v26
	v_lshl_add_u64 v[46:47], v[26:27], 0, s[62:63]
	s_nop 0
	v_addc_co_u32_e32 v33, vcc, 0, v27, vcc
	global_load_dwordx4 v[18:21], v[30:31], off offset:32
	global_load_dwordx4 v[22:25], v[30:31], off offset:16
	s_nop 0
	global_load_dwordx4 v[26:29], v[28:29], off offset:1024
	s_nop 0
	global_load_dwordx4 v[38:41], v[32:33], off offset:1024
	global_load_dwordx4 v[34:37], v[46:47], off offset:48
	global_load_dwordx4 v[42:45], v[46:47], off offset:32
	s_nop 0
	global_load_dwordx4 v[30:33], v[30:31], off offset:48
	s_nop 0
	global_load_dwordx4 v[46:49], v[46:47], off offset:16
	s_barrier
	ds_write_b128 v194, v[82:85]
	ds_write_b128 v194, v[86:89] offset:33280
	ds_write_b128 v194, v[90:93] offset:16
	ds_write_b128 v194, v[94:97] offset:33296
	ds_write_b128 v194, v[102:105] offset:32
	ds_write_b128 v194, v[106:109] offset:33312
	ds_write_b128 v194, v[110:113] offset:48
	ds_write_b128 v194, v[114:117] offset:33328
	s_waitcnt lgkmcnt(0)
	s_barrier
	ds_read_b128 v[82:85], v195
	ds_read_b128 v[86:89], v195 offset:32
	s_waitcnt vmcnt(19) lgkmcnt(1)
	v_mfma_f32_32x32x16_bf16 v[2:17], v[74:77], v[82:85], v[2:17]
	ds_read_b128 v[90:93], v195 offset:33280
	ds_read_b128 v[94:97], v195 offset:33312
	s_add_u32 s12, s12, 0x200
	s_addc_u32 s13, s13, 0
	v_lshl_add_u64 v[142:143], v[142:143], 0, s[66:67]
	v_add_u32_e32 v204, 0x2100, v204
	v_lshl_add_u64 v[146:147], v[146:147], 0, s[64:65]
	s_cmpk_eq_i32 s12, 0x800
	s_waitcnt lgkmcnt(1)
	v_mfma_f32_32x32x16_bf16 v[2:17], v[74:77], v[90:93], v[2:17]
	v_mul_f32_e64 v74, v152, v152
	v_mul_f32_e64 v75, v153, v153
	v_mul_f32_e64 v76, v154, v154
	v_mul_f32_e64 v77, v155, v155
	v_mul_f32_e32 v90, v174, v174
	v_add_u32_e32 v122, 0x800, v122
	s_waitcnt vmcnt(17)
	v_mfma_f32_32x32x16_bf16 v[2:17], v[78:81], v[82:85], v[2:17]
	v_pk_mov_b32 v[78:79], v[76:77], v[74:75] op_sel:[1,0]
	v_mov_b32_e32 v77, v75
	v_pk_add_f32 v[74:75], v[78:79], v[76:77]
	v_mov_b32_e32 v79, v162
	v_mov_b32_e32 v162, v167
	v_mul_f32_e32 v76, v165, v165
	v_mov_b32_e32 v78, v166
	v_mfma_f32_32x32x16_bf16 v[2:17], v[70:73], v[86:89], v[2:17]
	v_mul_f32_e64 v80, v162, v162
	v_mul_f32_e64 v81, v163, v163
	v_pk_fma_f32 v[76:77], v[164:165], v[164:165], v[76:77] op_sel_hi:[1,1,0]
	v_pk_fma_f32 v[78:79], v[78:79], v[78:79], v[80:81]
	s_nop 0
	v_pk_add_f32 v[76:77], v[78:79], v[76:77] op_sel:[1,0] op_sel_hi:[0,1]
	v_pk_add_f32 v[82:83], v[78:79], v[76:77]
	v_mul_f32_e32 v76, v170, v170
	s_waitcnt lgkmcnt(0)
	v_mfma_f32_32x32x16_bf16 v[2:17], v[70:73], v[94:97], v[2:17]
	v_mul_f32_e32 v70, v176, v176
	v_fma_f32 v78, v176, v176, v70
	v_fma_f32 v79, v177, v177, v70
	v_mov_b32_e32 v71, v168
	v_mov_b32_e32 v168, v159
	v_mov_b32_e32 v70, v158
	v_mul_f32_e32 v77, v171, v171
	v_mov_b32_e32 v145, v79
	s_waitcnt vmcnt(16)
	v_mfma_f32_32x32x16_bf16 v[2:17], v[66:69], v[86:89], v[2:17]
	v_mul_f32_e64 v66, v168, v168
	v_mul_f32_e64 v67, v169, v169
	v_add_f32_e64 v86, v74, v75
	v_add_f32_e64 v87, v75, v74
	v_fma_f32 v80, v70, v70, v66
	v_fma_f32 v81, v71, v71, v67
	ds_read_b128 v[66:69], v195 offset:64
	v_mul_f32_e32 v70, v157, v157
	v_pk_fma_f32 v[84:85], v[156:157], v[156:157], v[70:71] op_sel_hi:[1,1,0]
	ds_read_b128 v[70:73], v195 offset:96
	s_waitcnt vmcnt(15) lgkmcnt(1)
	v_mfma_f32_32x32x16_bf16 v[2:17], v[62:65], v[66:69], v[2:17]
	v_mov_b32_e32 v85, v76
	v_mov_b32_e32 v87, v77
	ds_read_b128 v[74:77], v195 offset:33344
	v_add_f32_e64 v84, v84, v86
	v_add_f32_e64 v85, v85, v87
	v_mul_f32_e32 v83, v175, v175
	v_pk_add_f32 v[84:85], v[80:81], v[84:85]
	ds_read_b128 v[78:81], v195 offset:33376
	s_waitcnt lgkmcnt(1)
	v_mfma_f32_32x32x16_bf16 v[2:17], v[62:65], v[74:77], v[2:17]
	v_mul_f32_e32 v64, v161, v161
	v_pk_fma_f32 v[64:65], v[160:161], v[160:161], v[64:65] op_sel_hi:[1,1,0]
	v_pk_add_f32 v[62:63], v[144:145], v[84:85]
	v_mov_b32_e32 v65, v90
	v_pk_add_f32 v[64:65], v[64:65], v[82:83]
	s_nop 0
	v_pk_add_f32 v[62:63], v[64:65], v[62:63]
	s_waitcnt vmcnt(13)
	v_mfma_f32_32x32x16_bf16 v[2:17], v[58:61], v[66:69], v[2:17]
	v_mul_f32_e64 v64, v180, v180
	v_mul_f32_e64 v65, v181, v181
	v_mul_f32_e64 v58, v178, v178
	v_mul_f32_e64 v59, v179, v179
	v_add_f32_e32 v62, v62, v63
	v_pk_mov_b32 v[60:61], v[58:59], v[64:65] op_sel:[1,0]
	v_mov_b32_e32 v59, v65
	v_pk_add_f32 v[58:59], v[60:61], v[58:59]
	v_pk_mul_f32 v[60:61], v[182:183], v[182:183]
	v_mfma_f32_32x32x16_bf16 v[2:17], v[54:57], v[70:73], v[2:17]
	v_mul_f32_e64 v64, v184, v184
	v_mul_f32_e64 v65, v185, v185
	v_mov_b32_e32 v66, v60
	v_mov_b32_e32 v67, v64
	v_mov_b32_e32 v64, v61
	v_pk_add_f32 v[60:61], v[66:67], v[64:65]
	v_add_f32_e32 v58, v58, v59
	v_add_f32_e32 v58, v61, v58
	s_waitcnt lgkmcnt(0)
	v_mfma_f32_32x32x16_bf16 v[2:17], v[54:57], v[78:81], v[2:17]
	v_add_f32_e32 v58, v60, v58
	v_add_f32_e32 v144, v62, v58
	s_waitcnt vmcnt(12)
	v_mfma_f32_32x32x16_bf16 v[2:17], v[50:53], v[70:73], v[2:17]
	s_cbranch_scc1 .LBB0_1234
	s_branch .LBB0_1232
